# v12 + diff-attention masked-tile loop trims: hoisted lane-swap index, no self-max, straight-line rescale tests, causal compares against one distance register with inline constants
# speedup vs baseline: 1.0049x; 1.0012x over previous
.LBB0_870:
	v_exp_f32_e32 v194, v174
	v_exp_f32_e32 v196, v172
	v_exp_f32_e32 v195, v175
	v_exp_f32_e32 v173, v173
	v_exp_f32_e32 v197, v168
	v_exp_f32_e32 v217, v170
	v_exp_f32_e32 v169, v169
	v_exp_f32_e32 v218, v171
	v_exp_f32_e32 v144, v149
	v_exp_f32_e32 v149, v146
	v_exp_f32_e32 v146, v4
	v_add_f32_e32 v4, v196, v194
	v_exp_f32_e32 v170, v164
	v_exp_f32_e32 v219, v166
	v_exp_f32_e32 v143, v154
	v_exp_f32_e32 v154, v148
	v_exp_f32_e32 v148, v10
	v_exp_f32_e32 v172, v5
	v_add_f32_e32 v5, v173, v195
	v_exp_f32_e32 v10, v165
	v_exp_f32_e32 v128, v167
	v_add_f32_e32 v4, v5, v4
	v_add_f32_e32 v5, v217, v197
	v_add_f32_e32 v4, v5, v4
	v_add_f32_e32 v5, v218, v169
	v_exp_f32_e32 v2, v11
	v_add_f32_e32 v11, v5, v4
	v_add_f32_e32 v129, v219, v170
	v_pk_add_f32 v[4:5], v[128:129], v[10:11]
	v_exp_f32_e32 v11, v134
	v_pk_add_f32 v[138:139], v[4:5], v[4:5] op_sel_hi:[0,1]
	v_exp_f32_e32 v129, v136
	v_exp_f32_e32 v138, v135
	v_exp_f32_e32 v134, v137
	v_exp_f32_e32 v142, v152
	v_add_f32_e32 v135, v129, v11
	v_exp_f32_e32 v152, v153
	v_exp_f32_e32 v153, v155
	v_exp_f32_e32 v145, v151
	v_exp_f32_e32 v155, v6
	v_exp_f32_e32 v151, v7
	v_pk_add_f32 v[6:7], v[134:135], v[138:139]
	v_exp_f32_e32 v135, v130
	v_pk_add_f32 v[136:137], v[6:7], v[6:7] op_sel_hi:[0,1]
	v_exp_f32_e32 v220, v132
	v_exp_f32_e32 v136, v131
	v_exp_f32_e32 v126, v133
	v_exp_f32_e32 v140, v8
	v_add_f32_e32 v127, v220, v135
	v_exp_f32_e32 v141, v9
	v_pk_add_f32 v[8:9], v[126:127], v[136:137]
	v_exp_f32_e32 v127, v124
	v_pk_add_f32 v[130:131], v[8:9], v[8:9] op_sel_hi:[0,1]
	v_exp_f32_e32 v221, v122
	v_exp_f32_e32 v130, v125
	v_exp_f32_e32 v174, v123
	v_add_u32_e32 v222, s83, v201
	v_add_f32_e32 v175, v221, v127
	v_exp_f32_e32 v162, v162
	v_exp_f32_e32 v163, v163
	v_exp_f32_e32 v156, v156
	v_exp_f32_e32 v157, v157
	ds_read_b64_tr_b16 v[164:165], v222 offset:9216
	ds_read_b64_tr_b16 v[166:167], v222 offset:9728
	v_pk_add_f32 v[122:123], v[174:175], v[130:131]
	v_exp_f32_e32 v131, v120
	v_pk_add_f32 v[132:133], v[122:123], v[122:123] op_sel_hi:[0,1]
	v_exp_f32_e32 v175, v116
	v_exp_f32_e32 v132, v121
	v_cvt_pk_bf16_f32 v168, v194, v195
	v_exp_f32_e32 v194, v117
	v_cvt_pk_bf16_f32 v4, v162, v163
	v_cvt_pk_bf16_f32 v5, v156, v157
	v_cvt_pk_bf16_f32 v6, v142, v152
	v_cvt_pk_bf16_f32 v7, v154, v144
	v_cvt_pk_bf16_f32 v169, v197, v169
	v_cvt_pk_bf16_f32 v170, v170, v10
	v_cvt_pk_bf16_f32 v171, v11, v138
	s_waitcnt lgkmcnt(0)
	v_mfma_f32_32x32x16_bf16 v[18:33], v[164:167], v[4:7], v[18:33]
	v_add_f32_e32 v195, v175, v131
	v_add_f32_e64 v116, v194, v132
	v_add_f32_e64 v117, v195, v133
	ds_read_b64_tr_b16 v[122:123], v222 offset:10240
	ds_read_b64_tr_b16 v[124:125], v222 offset:10752
	v_pk_add_f32 v[120:121], v[116:117], v[116:117] op_sel_hi:[0,1]
	v_exp_f32_e32 v195, v114
	v_exp_f32_e32 v120, v115
	v_cvt_pk_bf16_f32 v8, v148, v2
	v_mfma_f32_32x32x16_bf16 v[34:49], v[164:167], v[168:171], v[34:49]
	v_cvt_pk_bf16_f32 v9, v140, v141
	v_cvt_pk_bf16_f32 v10, v146, v172
	v_cvt_pk_bf16_f32 v11, v155, v151
	v_cvt_pk_bf16_f32 v136, v135, v136
	v_cvt_pk_bf16_f32 v137, v127, v130
	v_cvt_pk_bf16_f32 v138, v131, v132
	v_cvt_pk_bf16_f32 v139, v195, v120
	s_waitcnt lgkmcnt(0)
	v_mfma_f32_32x32x16_bf16 v[18:33], v[122:125], v[8:11], v[18:33]
	v_exp_f32_e32 v160, v160
	v_exp_f32_e32 v161, v161
	v_exp_f32_e32 v158, v158
	v_exp_f32_e32 v159, v159
	v_exp_f32_e32 v150, v150
	ds_read_b64_tr_b16 v[130:131], v222 offset:11264
	ds_read_b64_tr_b16 v[132:133], v222 offset:11776
	v_cvt_pk_bf16_f32 v114, v160, v161
	v_mfma_f32_32x32x16_bf16 v[34:49], v[122:125], v[136:139], v[34:49]
	v_cvt_pk_bf16_f32 v115, v158, v159
	v_cvt_pk_bf16_f32 v116, v143, v153
	v_cvt_pk_bf16_f32 v117, v150, v145
	v_cvt_pk_bf16_f32 v164, v196, v173
	v_cvt_pk_bf16_f32 v165, v217, v218
	v_cvt_pk_bf16_f32 v166, v219, v128
	v_cvt_pk_bf16_f32 v167, v129, v134
	s_waitcnt lgkmcnt(0)
	v_mfma_f32_32x32x16_bf16 v[18:33], v[130:133], v[114:117], v[18:33]
	v_exp_f32_e32 v135, v147
	ds_read_b64_tr_b16 v[122:123], v222 offset:12288
	ds_read_b64_tr_b16 v[124:125], v222 offset:12800
	v_exp_f32_e32 v147, v12
	v_exp_f32_e32 v197, v13
	v_exp_f32_e32 v223, v14
	v_exp_f32_e32 v134, v15
	v_exp_f32_e32 v173, v16
	v_mfma_f32_32x32x16_bf16 v[34:49], v[130:133], v[164:167], v[34:49]
	v_exp_f32_e32 v17, v17
	v_exp_f32_e32 v118, v118
	v_exp_f32_e32 v16, v119
	v_cvt_pk_bf16_f32 v12, v149, v135
	v_cvt_pk_bf16_f32 v13, v147, v197
	v_cvt_pk_bf16_f32 v14, v223, v134
	v_cvt_pk_bf16_f32 v15, v173, v17
	v_cvt_pk_bf16_f32 v126, v220, v126
	v_cvt_pk_bf16_f32 v127, v221, v174
	v_cvt_pk_bf16_f32 v128, v175, v194
	v_cvt_pk_bf16_f32 v129, v118, v16
	s_waitcnt lgkmcnt(0)
	v_mfma_f32_32x32x16_bf16 v[18:33], v[122:125], v[12:15], v[18:33]
	v_add_f32_e32 v2, v135, v2
	s_add_i32 s0, s91, 1
	s_and_b32 s91, s0, 3
	s_add_i32 s0, s74, 1
	s_and_b32 s74, s0, 3
	s_add_i32 s82, s82, 1
	s_cmp_ge_i32 s82, s68
	v_mfma_f32_32x32x16_bf16 v[34:49], v[122:125], v[126:129], v[34:49]
	ds_read_b64_tr_b16 v[122:123], v222 offset:13312
	ds_read_b64_tr_b16 v[124:125], v222 offset:13824
	ds_read_b64_tr_b16 v[130:131], v222 offset:14336
	ds_read_b64_tr_b16 v[132:133], v222 offset:14848
	v_add_u32_e32 v177, 64, v177
	s_waitcnt lgkmcnt(2)
	v_mfma_f32_32x32x16_bf16 v[50:65], v[122:125], v[4:7], v[50:65]
	v_add_f32_e32 v4, v160, v162
	v_add_f32_e32 v5, v161, v163
	v_add_f32_e32 v4, v5, v4
	v_add_f32_e32 v5, v158, v156
	v_add_f32_e32 v4, v5, v4
	v_add_f32_e32 v5, v159, v157
	v_mfma_f32_32x32x16_bf16 v[66:81], v[122:125], v[168:171], v[66:81]
	v_add_f32_e32 v4, v5, v4
	v_add_f32_e32 v5, v143, v142
	v_add_f32_e32 v4, v5, v4
	v_add_f32_e32 v5, v153, v152
	s_waitcnt lgkmcnt(0)
	v_mfma_f32_32x32x16_bf16 v[50:65], v[130:133], v[8:11], v[50:65]
	v_add_f32_e32 v8, v5, v4
	ds_read_b64_tr_b16 v[4:5], v222 offset:15360
	ds_read_b64_tr_b16 v[6:7], v222 offset:15872
	v_add_f32_e32 v9, v150, v154
	v_add_f32_e32 v8, v9, v8
	v_add_f32_e32 v9, v145, v144
	v_add_f32_e32 v8, v9, v8
	v_add_f32_e32 v9, v149, v148
	v_mfma_f32_32x32x16_bf16 v[66:81], v[130:133], v[136:139], v[66:81]
	v_add_f32_e32 v119, v9, v8
	ds_read_b64_tr_b16 v[8:9], v222 offset:16384
	ds_read_b64_tr_b16 v[10:11], v222 offset:16896
	v_add_f32_e32 v2, v2, v119
	s_waitcnt vmcnt(6) lgkmcnt(0)
	s_barrier
	s_waitcnt lgkmcnt(2)
	v_mfma_f32_32x32x16_bf16 v[50:65], v[4:7], v[114:117], v[50:65]
	v_add_f32_e32 v114, v147, v140
	v_add_f32_e32 v2, v114, v2
	v_add_f32_e32 v114, v197, v141
	v_add_f32_e32 v2, v114, v2
	v_add_f32_e32 v114, v223, v146
	v_add_f32_e32 v2, v114, v2
	v_mfma_f32_32x32x16_bf16 v[66:81], v[4:7], v[164:167], v[66:81]
	v_add_f32_e32 v4, v134, v172
	v_add_f32_e32 v2, v4, v2
	v_add_f32_e32 v4, v173, v155
	v_add_f32_e32 v2, v4, v2
	v_add_f32_e32 v4, v17, v151
	v_add_f32_e32 v17, v118, v195
	v_add_f32_e32 v2, v4, v2
	s_waitcnt lgkmcnt(0)
	v_mfma_f32_32x32x16_bf16 v[50:65], v[8:11], v[12:15], v[50:65]
	v_add_f32_e64 v4, v16, v120
	v_add_f32_e64 v5, v17, v121
	v_add_f32_e32 v214, v214, v2
	v_add_f32_e32 v2, v4, v5
	v_add_f32_e32 v209, v209, v2
	v_mfma_f32_32x32x16_bf16 v[66:81], v[8:11], v[126:129], v[66:81]
	s_cbranch_scc1 .LBB0_899

.LBB0_883:
	s_mul_i32 s2, s74, 0x4400
	s_add_i32 s83, s2, 0
	v_add_u32_e32 v164, s83, v207
	s_cmp_lg_u32 s82, -1
	ds_read_b128 v[4:7], v164 offset:4608
	ds_read_b128 v[8:11], v164
	ds_read_b128 v[12:15], v164 offset:32
	ds_read_b128 v[146:149], v164 offset:4640
	s_cselect_b64 s[88:89], -1, 0
	v_sub_u32_e32 v2, v177, v176
	v_cmp_gt_i32_e64 s[2:3], v2, 59
	v_cmp_lt_i32_e64 s[6:7], v2, 59
	v_cmp_gt_i32_e64 s[24:25], v2, 18
	s_waitcnt lgkmcnt(2)
	v_mfma_f32_32x32x16_bf16 v[130:145], v[8:11], v[178:181], v[98:113]
	v_cmp_gt_i32_e64 s[26:27], v2, 49
	v_mfma_f32_32x32x16_bf16 v[114:129], v[4:7], v[178:181], v[98:113]
	v_cmp_gt_i32_e64 s[28:29], v2, 17
	v_cmp_gt_i32_e64 s[30:31], v2, 48
	v_cmp_gt_i32_e64 s[34:35], v2, 16
	v_cmp_gt_i32_e64 s[36:37], v2, 43
	v_cmp_gt_i32_e64 s[38:39], v2, 11
	v_cmp_gt_i32_e64 s[40:41], v2, 42
	v_cmp_gt_i32_e64 s[42:43], v2, 10
	s_waitcnt lgkmcnt(1)
	v_mfma_f32_32x32x16_bf16 v[130:145], v[12:15], v[182:185], v[130:145]
	v_cmp_gt_i32_e64 s[44:45], v2, 41
	v_cmp_gt_i32_e64 s[46:47], v2, 9
	v_cmp_gt_i32_e64 s[48:49], v2, 40
	v_cmp_gt_i32_e64 s[50:51], v2, 8
	s_waitcnt lgkmcnt(0)
	v_mfma_f32_32x32x16_bf16 v[114:129], v[146:149], v[182:185], v[114:129]
	v_cmp_gt_i32_e64 s[52:53], v2, 35
	v_cmp_gt_i32_e64 s[54:55], v2, 3
	v_cmp_gt_i32_e64 s[56:57], v2, 34
	v_cmp_gt_i32_e64 s[58:59], v2, 2
	v_cmp_gt_i32_e64 s[8:9], v2, 26
	v_cmp_gt_i32_e64 s[10:11], v2, 57
	v_cmp_gt_i32_e64 s[12:13], v2, 25
	v_cmp_gt_i32_e64 s[14:15], v2, 56
	v_cmp_gt_i32_e64 s[16:17], v2, 24
	v_cmp_gt_i32_e64 s[18:19], v2, 51
	v_cmp_gt_i32_e64 s[20:21], v2, 19
	v_cmp_gt_i32_e64 s[22:23], v2, 50
	v_cmp_gt_i32_e64 s[4:5], v2, 27
	v_cndmask_b32_e64 v4, v130, v243, s[2:3]
	v_cmp_gt_i32_e64 s[60:61], v2, 33
	v_cndmask_b32_e64 v160, v114, v243, s[4:5]
	v_cndmask_b32_e64 v162, v4, v130, s[6:7]
	v_cndmask_b32_e64 v163, v243, v131, s[6:7]
	v_cndmask_b32_e64 v161, v115, v243, s[8:9]
	v_cndmask_b32_e64 v156, v132, v243, s[10:11]
	v_cndmask_b32_e64 v158, v116, v243, s[12:13]
	v_cmp_gt_i32_e64 s[62:63], v2, 1
	v_cndmask_b32_e64 v157, v133, v243, s[14:15]
	v_cndmask_b32_e64 v159, v117, v243, s[16:17]
	v_cndmask_b32_e64 v152, v134, v243, s[18:19]
	v_cndmask_b32_e64 v154, v118, v243, s[20:21]
	v_cmp_gt_i32_e64 s[64:65], v2, 32
	v_max3_f32 v2, v162, v163, v156
	v_max3_f32 v114, v160, v161, v158
	v_cndmask_b32_e64 v153, v135, v243, s[22:23]
	v_cndmask_b32_e64 v155, v119, v243, s[24:25]
	v_cndmask_b32_e64 v148, v136, v243, s[26:27]
	v_cndmask_b32_e64 v150, v120, v243, s[28:29]
	v_max3_f32 v2, v2, v157, v152
	v_max3_f32 v114, v114, v159, v154
	v_cndmask_b32_e64 v149, v137, v243, s[30:31]
	v_cndmask_b32_e64 v151, v121, v243, s[34:35]
	v_cndmask_b32_e64 v10, v138, v243, s[36:37]
	v_cndmask_b32_e64 v146, v122, v243, s[38:39]
	v_max3_f32 v2, v2, v153, v148
	v_max3_f32 v114, v114, v155, v150
	v_cndmask_b32_e64 v11, v139, v243, s[40:41]
	v_cndmask_b32_e64 v147, v123, v243, s[42:43]
	v_cndmask_b32_e64 v8, v140, v243, s[44:45]
	v_cndmask_b32_e64 v12, v124, v243, s[46:47]
	v_cmp_gt_i32_e64 s[66:67], v177, v176
	v_max3_f32 v2, v2, v149, v10
	v_max3_f32 v114, v114, v151, v146
	v_cndmask_b32_e64 v9, v141, v243, s[48:49]
	v_cndmask_b32_e64 v13, v125, v243, s[50:51]
	v_cndmask_b32_e64 v4, v142, v243, s[52:53]
	v_cndmask_b32_e64 v14, v126, v243, s[54:55]
	v_cndmask_b32_e64 v7, v145, v243, s[64:65]
	v_cndmask_b32_e64 v17, v129, v243, s[66:67]
	v_max3_f32 v2, v2, v11, v8
	v_max3_f32 v114, v114, v147, v12
	v_cndmask_b32_e64 v5, v143, v243, s[56:57]
	v_cndmask_b32_e64 v15, v127, v243, s[58:59]
	v_cndmask_b32_e64 v6, v144, v243, s[60:61]
	v_cndmask_b32_e64 v16, v128, v243, s[62:63]
	v_max3_f32 v2, v2, v9, v4
	v_max3_f32 v114, v114, v13, v14
	v_max3_f32 v2, v2, v5, v6
	v_max3_f32 v114, v114, v15, v16
	v_max_f32_e32 v115, v7, v17
	v_max3_f32 v2, v2, v114, v115
	ds_bpermute_b32 v114, v230, v2
	s_and_b64 vcc, exec, s[88:89]
	s_waitcnt lgkmcnt(0)
	v_max_f32_e32 v114, v2, v114
	s_cbranch_vccz .Ldm0_first
	v_cmp_lt_f32_e32 vcc, s94, v114
	s_mov_b64 s[94:95], s[84:85]
	s_cbranch_vccz .LBB0_890
	v_max_f32_e32 v2, v114, v114
	v_max_f32_e32 v2, 0, v2
	s_branch .Ldm0_resc
.Ldm0_first:
	s_mov_b64 s[94:95], s[84:85]
	v_mov_b32_e32 v2, v114
.Ldm0_resc:
	v_exp_f32_e64 v100, -v2
	v_add_f32_e32 v216, v216, v2
	v_xor_b32_e32 v98, 0x80000000, v216
	v_pk_add_f32 v[162:163], v[162:163], v[2:3] op_sel_hi:[1,0] neg_lo:[0,1] neg_hi:[0,1]
	v_mul_f32_e32 v214, v214, v100
	v_pk_add_f32 v[160:161], v[160:161], v[2:3] op_sel_hi:[1,0] neg_lo:[0,1] neg_hi:[0,1]
	v_pk_add_f32 v[156:157], v[156:157], v[2:3] op_sel_hi:[1,0] neg_lo:[0,1] neg_hi:[0,1]
	v_pk_add_f32 v[158:159], v[158:159], v[2:3] op_sel_hi:[1,0] neg_lo:[0,1] neg_hi:[0,1]
	v_pk_add_f32 v[152:153], v[152:153], v[2:3] op_sel_hi:[1,0] neg_lo:[0,1] neg_hi:[0,1]
	v_pk_add_f32 v[154:155], v[154:155], v[2:3] op_sel_hi:[1,0] neg_lo:[0,1] neg_hi:[0,1]
	v_pk_add_f32 v[148:149], v[148:149], v[2:3] op_sel_hi:[1,0] neg_lo:[0,1] neg_hi:[0,1]
	v_pk_add_f32 v[150:151], v[150:151], v[2:3] op_sel_hi:[1,0] neg_lo:[0,1] neg_hi:[0,1]
	v_pk_add_f32 v[10:11], v[10:11], v[2:3] op_sel_hi:[1,0] neg_lo:[0,1] neg_hi:[0,1]
	v_pk_add_f32 v[146:147], v[146:147], v[2:3] op_sel_hi:[1,0] neg_lo:[0,1] neg_hi:[0,1]
	v_pk_add_f32 v[8:9], v[8:9], v[2:3] op_sel_hi:[1,0] neg_lo:[0,1] neg_hi:[0,1]
	v_pk_add_f32 v[12:13], v[12:13], v[2:3] op_sel_hi:[1,0] neg_lo:[0,1] neg_hi:[0,1]
	v_pk_add_f32 v[4:5], v[4:5], v[2:3] op_sel_hi:[1,0] neg_lo:[0,1] neg_hi:[0,1]
	v_pk_add_f32 v[14:15], v[14:15], v[2:3] op_sel_hi:[1,0] neg_lo:[0,1] neg_hi:[0,1]
	v_pk_add_f32 v[6:7], v[6:7], v[2:3] op_sel_hi:[1,0] neg_lo:[0,1] neg_hi:[0,1]
	v_pk_add_f32 v[16:17], v[16:17], v[2:3] op_sel_hi:[1,0] neg_lo:[0,1] neg_hi:[0,1]
	v_pk_mul_f32 v[32:33], v[32:33], v[100:101] op_sel_hi:[1,0]
	v_pk_mul_f32 v[30:31], v[30:31], v[100:101] op_sel_hi:[1,0]
	v_pk_mul_f32 v[28:29], v[28:29], v[100:101] op_sel_hi:[1,0]
	v_pk_mul_f32 v[26:27], v[26:27], v[100:101] op_sel_hi:[1,0]
	v_pk_mul_f32 v[24:25], v[24:25], v[100:101] op_sel_hi:[1,0]
	v_pk_mul_f32 v[22:23], v[22:23], v[100:101] op_sel_hi:[1,0]
	v_pk_mul_f32 v[20:21], v[20:21], v[100:101] op_sel_hi:[1,0]
	v_pk_mul_f32 v[18:19], v[18:19], v[100:101] op_sel_hi:[1,0]
	v_pk_mul_f32 v[64:65], v[64:65], v[100:101] op_sel_hi:[1,0]
	v_pk_mul_f32 v[62:63], v[62:63], v[100:101] op_sel_hi:[1,0]
	v_pk_mul_f32 v[60:61], v[60:61], v[100:101] op_sel_hi:[1,0]
	v_pk_mul_f32 v[58:59], v[58:59], v[100:101] op_sel_hi:[1,0]
	v_pk_mul_f32 v[56:57], v[56:57], v[100:101] op_sel_hi:[1,0]
	v_pk_mul_f32 v[54:55], v[54:55], v[100:101] op_sel_hi:[1,0]
	v_pk_mul_f32 v[52:53], v[52:53], v[100:101] op_sel_hi:[1,0]
	v_pk_mul_f32 v[50:51], v[50:51], v[100:101] op_sel_hi:[1,0]
	v_mov_b32_e32 v99, v98
	v_mov_b32_e32 v100, v98
	v_mov_b32_e32 v101, v98
	v_mov_b32_e32 v102, v98
	v_mov_b32_e32 v103, v98
	v_mov_b32_e32 v104, v98
	v_mov_b32_e32 v105, v98
	v_mov_b32_e32 v106, v98
	v_mov_b32_e32 v107, v98
	v_mov_b32_e32 v108, v98
	v_mov_b32_e32 v109, v98
	v_mov_b32_e32 v110, v98
	v_mov_b32_e32 v111, v98
	v_mov_b32_e32 v112, v98
	v_mov_b32_e32 v113, v98
.LBB0_890:
	ds_read_b128 v[130:133], v164 offset:64
	ds_read_b128 v[166:169], v164 offset:96
	ds_read_b128 v[170:173], v164 offset:4672
	ds_read_b128 v[194:197], v164 offset:4704
	s_mov_b32 s85, 0x800000
	s_mov_b32 s0, 0x41800000
	s_waitcnt lgkmcnt(3)
	v_mfma_f32_32x32x16_bf16 v[114:129], v[130:133], v[186:189], v[82:97]
	s_waitcnt lgkmcnt(2)
	v_mfma_f32_32x32x16_bf16 v[114:129], v[166:169], v[190:193], v[114:129]
	s_and_b64 vcc, exec, s[88:89]
	s_waitcnt lgkmcnt(1)
	v_mfma_f32_32x32x16_bf16 v[130:145], v[170:173], v[186:189], v[82:97]
	s_nop 8
	v_cndmask_b32_e64 v2, v114, v243, s[2:3]
	v_cndmask_b32_e64 v174, v2, v114, s[6:7]
	v_cndmask_b32_e64 v175, v243, v115, s[6:7]
	v_cndmask_b32_e64 v168, v116, v243, s[10:11]
	v_cndmask_b32_e64 v169, v117, v243, s[14:15]
	v_cndmask_b32_e64 v164, v118, v243, s[18:19]
	v_max3_f32 v2, v174, v175, v168
	s_waitcnt lgkmcnt(0)
	v_mfma_f32_32x32x16_bf16 v[130:145], v[194:197], v[190:193], v[130:145]
	v_cndmask_b32_e64 v165, v119, v243, s[22:23]
	v_max3_f32 v2, v2, v169, v164
	v_cndmask_b32_e64 v124, v124, v243, s[44:45]
	v_cndmask_b32_e64 v125, v125, v243, s[48:49]
	v_cndmask_b32_e64 v115, v129, v243, s[64:65]
	v_cndmask_b32_e64 v114, v128, v243, s[60:61]
	s_nop 5
	v_cndmask_b32_e64 v172, v130, v243, s[4:5]
	v_cndmask_b32_e64 v173, v131, v243, s[8:9]
	v_cndmask_b32_e64 v170, v132, v243, s[12:13]
	v_cndmask_b32_e64 v171, v133, v243, s[16:17]
	v_cndmask_b32_e64 v166, v134, v243, s[20:21]
	v_cndmask_b32_e64 v134, v120, v243, s[26:27]
	v_cndmask_b32_e64 v120, v126, v243, s[52:53]
	v_max3_f32 v126, v172, v173, v170
	v_cndmask_b32_e64 v167, v135, v243, s[24:25]
	v_cndmask_b32_e64 v136, v136, v243, s[28:29]
	v_max3_f32 v126, v126, v171, v166
	v_cndmask_b32_e64 v135, v121, v243, s[30:31]
	v_cndmask_b32_e64 v137, v137, v243, s[34:35]
	v_cndmask_b32_e64 v130, v122, v243, s[36:37]
	v_cndmask_b32_e64 v132, v138, v243, s[38:39]
	v_max3_f32 v2, v2, v165, v134
	v_max3_f32 v126, v126, v167, v136
	v_cndmask_b32_e64 v131, v123, v243, s[40:41]
	v_cndmask_b32_e64 v133, v139, v243, s[42:43]
	v_cndmask_b32_e64 v122, v140, v243, s[46:47]
	v_max3_f32 v2, v2, v135, v130
	v_max3_f32 v126, v126, v137, v132
	v_cndmask_b32_e64 v123, v141, v243, s[50:51]
	v_cndmask_b32_e64 v116, v142, v243, s[54:55]
	v_cndmask_b32_e64 v119, v145, v243, s[66:67]
	v_max3_f32 v2, v2, v131, v124
	v_max3_f32 v126, v126, v133, v122
	v_cndmask_b32_e64 v121, v127, v243, s[56:57]
	v_cndmask_b32_e64 v117, v143, v243, s[58:59]
	v_cndmask_b32_e64 v118, v144, v243, s[62:63]
	v_max3_f32 v2, v2, v125, v120
	v_max3_f32 v126, v126, v123, v116
	v_max3_f32 v2, v2, v121, v114
	v_max3_f32 v126, v126, v117, v118
	v_max_f32_e32 v127, v115, v119
	v_max3_f32 v2, v2, v126, v127
	ds_bpermute_b32 v126, v230, v2
	s_waitcnt lgkmcnt(0)
	v_max_f32_e32 v126, v2, v126
	s_cbranch_vccz .Ldm1_first
	v_readlane_b32 s56, v255, 12
	v_cmp_lt_f32_e32 vcc, s0, v126
	v_readlane_b32 s57, v255, 13
	s_mov_b32 s55, 0xda24260
	s_cbranch_vccz .LBB0_870
	v_max_f32_e32 v2, v126, v126
	v_max_f32_e32 v2, 0, v2
	s_branch .Ldm1_resc
.Ldm1_first:
	v_readlane_b32 s56, v255, 12
	v_readlane_b32 s57, v255, 13
	s_mov_b32 s55, 0xda24260
	v_mov_b32_e32 v2, v126
.Ldm1_resc:
	v_exp_f32_e64 v84, -v2
	v_add_f32_e32 v215, v215, v2
	v_xor_b32_e32 v82, 0x80000000, v215
	v_pk_add_f32 v[174:175], v[174:175], v[2:3] op_sel_hi:[1,0] neg_lo:[0,1] neg_hi:[0,1]
	v_mul_f32_e32 v209, v209, v84
	v_pk_add_f32 v[172:173], v[172:173], v[2:3] op_sel_hi:[1,0] neg_lo:[0,1] neg_hi:[0,1]
	v_pk_add_f32 v[168:169], v[168:169], v[2:3] op_sel_hi:[1,0] neg_lo:[0,1] neg_hi:[0,1]
	v_pk_add_f32 v[170:171], v[170:171], v[2:3] op_sel_hi:[1,0] neg_lo:[0,1] neg_hi:[0,1]
	v_pk_add_f32 v[164:165], v[164:165], v[2:3] op_sel_hi:[1,0] neg_lo:[0,1] neg_hi:[0,1]
	v_pk_add_f32 v[166:167], v[166:167], v[2:3] op_sel_hi:[1,0] neg_lo:[0,1] neg_hi:[0,1]
	v_pk_add_f32 v[134:135], v[134:135], v[2:3] op_sel_hi:[1,0] neg_lo:[0,1] neg_hi:[0,1]
	v_pk_add_f32 v[136:137], v[136:137], v[2:3] op_sel_hi:[1,0] neg_lo:[0,1] neg_hi:[0,1]
	v_pk_add_f32 v[130:131], v[130:131], v[2:3] op_sel_hi:[1,0] neg_lo:[0,1] neg_hi:[0,1]
	v_pk_add_f32 v[132:133], v[132:133], v[2:3] op_sel_hi:[1,0] neg_lo:[0,1] neg_hi:[0,1]
	v_pk_add_f32 v[124:125], v[124:125], v[2:3] op_sel_hi:[1,0] neg_lo:[0,1] neg_hi:[0,1]
	v_pk_add_f32 v[122:123], v[122:123], v[2:3] op_sel_hi:[1,0] neg_lo:[0,1] neg_hi:[0,1]
	v_pk_add_f32 v[120:121], v[120:121], v[2:3] op_sel_hi:[1,0] neg_lo:[0,1] neg_hi:[0,1]
	v_pk_add_f32 v[116:117], v[116:117], v[2:3] op_sel_hi:[1,0] neg_lo:[0,1] neg_hi:[0,1]
	v_pk_add_f32 v[114:115], v[114:115], v[2:3] op_sel_hi:[1,0] neg_lo:[0,1] neg_hi:[0,1]
	v_pk_add_f32 v[118:119], v[118:119], v[2:3] op_sel_hi:[1,0] neg_lo:[0,1] neg_hi:[0,1]
	v_pk_mul_f32 v[48:49], v[48:49], v[84:85] op_sel_hi:[1,0]
	v_pk_mul_f32 v[46:47], v[46:47], v[84:85] op_sel_hi:[1,0]
	v_pk_mul_f32 v[44:45], v[44:45], v[84:85] op_sel_hi:[1,0]
	v_pk_mul_f32 v[42:43], v[42:43], v[84:85] op_sel_hi:[1,0]
	v_pk_mul_f32 v[40:41], v[40:41], v[84:85] op_sel_hi:[1,0]
	v_pk_mul_f32 v[38:39], v[38:39], v[84:85] op_sel_hi:[1,0]
	v_pk_mul_f32 v[36:37], v[36:37], v[84:85] op_sel_hi:[1,0]
	v_pk_mul_f32 v[34:35], v[34:35], v[84:85] op_sel_hi:[1,0]
	v_pk_mul_f32 v[80:81], v[80:81], v[84:85] op_sel_hi:[1,0]
	v_pk_mul_f32 v[78:79], v[78:79], v[84:85] op_sel_hi:[1,0]
	v_pk_mul_f32 v[76:77], v[76:77], v[84:85] op_sel_hi:[1,0]
	v_pk_mul_f32 v[74:75], v[74:75], v[84:85] op_sel_hi:[1,0]
	v_pk_mul_f32 v[72:73], v[72:73], v[84:85] op_sel_hi:[1,0]
	v_pk_mul_f32 v[70:71], v[70:71], v[84:85] op_sel_hi:[1,0]
	v_pk_mul_f32 v[68:69], v[68:69], v[84:85] op_sel_hi:[1,0]
	v_pk_mul_f32 v[66:67], v[66:67], v[84:85] op_sel_hi:[1,0]
	v_mov_b32_e32 v83, v82
	v_mov_b32_e32 v84, v82
	v_mov_b32_e32 v85, v82
	v_mov_b32_e32 v86, v82
	v_mov_b32_e32 v87, v82
	v_mov_b32_e32 v88, v82
	v_mov_b32_e32 v89, v82
	v_mov_b32_e32 v90, v82
	v_mov_b32_e32 v91, v82
	v_mov_b32_e32 v92, v82
	v_mov_b32_e32 v93, v82
	v_mov_b32_e32 v94, v82
	v_mov_b32_e32 v95, v82
	v_mov_b32_e32 v96, v82
	v_mov_b32_e32 v97, v82
	s_branch .LBB0_870
